# B3 invt: the six ROWSS row-partial loads per wave issued together before the reduce loop
# baseline (speedup 1.0000x reference)
.LBB0_1325:
	s_and_saveexec_b64 s[0:1], s[66:67]
	ds_write_b32 v23, v173
	s_or_b64 exec, exec, s[0:1]
	s_andn2_b64 vcc, exec, s[68:69]
	s_lshl_b32 s2, s91, 5
	s_cbranch_vccnz .LBB0_1336
	v_and_b32_e32 v0, 64, v188
	v_add_u32_e32 v5, 64, v0
	v_xor_b32_e32 v0, 1, v188
	v_cmp_lt_i32_e32 vcc, v0, v5
	v_xor_b32_e32 v1, 2, v188
	v_xor_b32_e32 v2, 4, v188
	v_cndmask_b32_e32 v0, v188, v0, vcc
	v_cmp_lt_i32_e32 vcc, v1, v5
	v_xor_b32_e32 v3, 8, v188
	v_xor_b32_e32 v4, 16, v188
	v_cndmask_b32_e32 v1, v188, v1, vcc
	v_cmp_lt_i32_e32 vcc, v2, v5
	v_xor_b32_e32 v6, 32, v188
	s_and_b32 s0, s2, 0x7e0
	v_cndmask_b32_e32 v2, v188, v2, vcc
	v_cmp_lt_i32_e32 vcc, v3, v5
	s_add_i32 s3, s2, -15
	v_lshlrev_b32_e32 v0, 2, v0
	v_cndmask_b32_e32 v3, v188, v3, vcc
	v_cmp_lt_i32_e32 vcc, v4, v5
	v_lshlrev_b32_e32 v1, 2, v1
	v_lshlrev_b32_e32 v2, 2, v2
	v_cndmask_b32_e32 v4, v188, v4, vcc
	v_cmp_lt_i32_e32 vcc, v6, v5
	v_lshlrev_b32_e32 v3, 2, v3
	v_lshlrev_b32_e32 v4, 2, v4
	v_cndmask_b32_e32 v5, v188, v6, vcc
	v_lshlrev_b32_e32 v5, 2, v5
	s_sub_i32 s8, 14, s0
	s_mov_b32 s9, s73
	s_mov_b32 s10, s64
	v_mov_b32_e32 v236, 0
	v_mov_b32_e32 v237, 0
	v_mov_b32_e32 v238, 0
	v_mov_b32_e32 v239, 0
	v_mov_b32_e32 v240, 0
	v_mov_b32_e32 v241, 0
	s_waitcnt lgkmcnt(0)
	s_and_saveexec_b64 s[0:1], s[38:39]
	s_add_i32 s11, s3, s64
	s_max_i32 s12, s11, 0
	s_min_i32 s12, s12, 0x1fff
	s_mov_b32 s13, s60
	s_lshl_b64 s[12:13], s[12:13], 7
	v_lshl_add_u64 v[6:7], v[16:17], 0, s[12:13]
	global_load_dword v236, v[6:7], off
	s_add_i32 s11, s11, 8
	s_max_i32 s12, s11, 0
	s_min_i32 s12, s12, 0x1fff
	s_mov_b32 s13, s60
	s_lshl_b64 s[12:13], s[12:13], 7
	v_lshl_add_u64 v[6:7], v[16:17], 0, s[12:13]
	global_load_dword v237, v[6:7], off
	s_add_i32 s11, s11, 8
	s_max_i32 s12, s11, 0
	s_min_i32 s12, s12, 0x1fff
	s_mov_b32 s13, s60
	s_lshl_b64 s[12:13], s[12:13], 7
	v_lshl_add_u64 v[6:7], v[16:17], 0, s[12:13]
	global_load_dword v238, v[6:7], off
	s_add_i32 s11, s11, 8
	s_max_i32 s12, s11, 0
	s_min_i32 s12, s12, 0x1fff
	s_mov_b32 s13, s60
	s_lshl_b64 s[12:13], s[12:13], 7
	v_lshl_add_u64 v[6:7], v[16:17], 0, s[12:13]
	global_load_dword v239, v[6:7], off
	s_add_i32 s11, s11, 8
	s_max_i32 s12, s11, 0
	s_min_i32 s12, s12, 0x1fff
	s_mov_b32 s13, s60
	s_lshl_b64 s[12:13], s[12:13], 7
	v_lshl_add_u64 v[6:7], v[16:17], 0, s[12:13]
	global_load_dword v240, v[6:7], off
	s_add_i32 s11, s11, 8
	s_max_i32 s12, s11, 0
	s_min_i32 s12, s12, 0x1fff
	s_mov_b32 s13, s60
	s_lshl_b64 s[12:13], s[12:13], 7
	v_lshl_add_u64 v[6:7], v[16:17], 0, s[12:13]
	global_load_dword v241, v[6:7], off
	s_add_i32 s11, s11, 8
	s_or_b64 exec, exec, s[0:1]
	s_branch .LBB0_1331

.LBB0_1331:
	s_waitcnt vmcnt(0)
	v_mov_b32_e32 v6, v236
	v_mov_b32_e32 v236, v237
	v_mov_b32_e32 v237, v238
	v_mov_b32_e32 v238, v239
	v_mov_b32_e32 v239, v240
	v_mov_b32_e32 v240, v241
.LBB0_1333:
	s_waitcnt vmcnt(0) lgkmcnt(0)
	ds_bpermute_b32 v7, v0, v6
	s_waitcnt lgkmcnt(0)
	v_add_f32_e32 v6, v6, v7
	ds_bpermute_b32 v7, v1, v6
	s_waitcnt lgkmcnt(0)
	v_add_f32_e32 v6, v6, v7
	ds_bpermute_b32 v7, v2, v6
	s_waitcnt lgkmcnt(0)
	v_add_f32_e32 v6, v6, v7
	ds_bpermute_b32 v7, v3, v6
	s_waitcnt lgkmcnt(0)
	v_add_f32_e32 v6, v6, v7
	ds_bpermute_b32 v7, v4, v6
	s_waitcnt lgkmcnt(0)
	v_add_f32_e32 v6, v6, v7
	ds_bpermute_b32 v7, v5, v6
	s_and_saveexec_b64 s[0:1], s[40:41]
	s_cbranch_execz .LBB0_1330
	s_cmp_le_i32 s10, s8
	v_mov_b32_e32 v8, 0
	s_cbranch_scc1 .LBB0_1329
	s_waitcnt lgkmcnt(0)
	v_add_f32_e32 v6, v6, v7
	v_fmamk_f32 v6, v6, 0x3a000000, v189
	v_mul_f32_e32 v7, 0x4f800000, v6
	v_cmp_gt_f32_e32 vcc, s84, v6
	s_nop 1
	v_cndmask_b32_e32 v6, v6, v7, vcc
	v_sqrt_f32_e32 v7, v6
	s_nop 0
	v_add_u32_e32 v8, -1, v7
	v_fma_f32 v10, -v8, v7, v6
	v_add_u32_e32 v9, 1, v7
	v_cmp_ge_f32_e64 s[46:47], 0, v10
	s_nop 1
	v_cndmask_b32_e64 v8, v7, v8, s[46:47]
	v_fma_f32 v7, -v9, v7, v6
	v_cmp_lt_f32_e64 s[46:47], 0, v7
	s_nop 1
	v_cndmask_b32_e64 v7, v8, v9, s[46:47]
	v_mul_f32_e32 v8, 0x37800000, v7
	v_cndmask_b32_e32 v7, v7, v8, vcc
	v_cmp_class_f32_e32 vcc, v6, v190
	s_nop 1
	v_cndmask_b32_e32 v6, v7, v6, vcc
	v_div_scale_f32 v7, s[12:13], v6, v6, 1.0
	v_rcp_f32_e32 v8, v7
	s_nop 0
	v_fma_f32 v9, -v7, v8, 1.0
	v_fmac_f32_e32 v8, v9, v8
	v_div_scale_f32 v9, vcc, 1.0, v6, 1.0
	v_mul_f32_e32 v10, v9, v8
	v_fma_f32 v11, -v7, v10, v9
	v_fmac_f32_e32 v10, v11, v8
	v_fma_f32 v7, -v7, v10, v9
	v_div_fmas_f32 v7, v7, v8, v10
	v_div_fixup_f32 v8, v7, v6, 1.0
	s_branch .LBB0_1329
